# pipelined release polling: each of the 32 barrier poll loops keeps two polls in flight (the wait before the compare covers the previous poll only), halving the sampling period
# baseline (speedup 1.0000x reference)
; __device__ __forceinline__ unsigned xb_ld(unsigned* p)              { return __hip_atomic_load(p, __ATOMIC_RELAXED, __HIP_MEMORY_SCOPE_AGENT); }
; __device__ __forceinline__ unsigned xb_add(unsigned* p, unsigned v) { return __hip_atomic_fetch_add(p, v, __ATOMIC_RELAXED, __HIP_MEMORY_SCOPE_AGENT); }
; #define XB_SPIN(cond, bar) do { unsigned _sp = 0; while (cond) { __builtin_amdgcn_s_sleep(1); \
;     if ((++_sp & 255u) == 0u) { if (xb_ld(&(bar)[XB_TMO])) break; if (_sp > XB_SPIN_CAP) { atomicAdd(&(bar)[XB_TMO], 1u); break; } } } } while (0)
; __device__ __forceinline__ void xcd_barrier(const XcdBarrier& b, const bool xb_leader) {
;     ...
;         const unsigned old = xb_add(&bar[XB_XSUB(b.x)], 1u);
;         const unsigned gen = old / nloc;
;         if (old + 1u == (gen + 1u) * nloc) {
;             __builtin_amdgcn_fence(__ATOMIC_RELEASE, "agent");
;             asm volatile("s_waitcnt vmcnt(0)" ::: "memory");
;             const unsigned og = xb_add(&bar[XB_TOP], 1u);
;             const unsigned tg = og / nx;
;             if (og + 1u == (tg + 1u) * nx) xb_add(&bar[XB_TOPGEN], 1u);
;             else XB_SPIN(xb_ld(&bar[XB_TOPGEN]) == tg, bar);
.LBB0_87:
	s_or_b64 exec, exec, s[12:13]
	v_cvt_f32_u32_e32 v2, v9
	s_waitcnt vmcnt(0)
	v_readfirstlane_b32 s3, v1
	v_sub_u32_e32 v1, 0, v9
	v_rcp_iflag_f32_e32 v2, v2
	v_add_u32_e32 v3, s3, v0
	v_mul_f32_e32 v2, 0x4f7ffffe, v2
	v_cvt_u32_f32_e32 v2, v2
	v_mul_lo_u32 v0, v1, v2
	v_mul_hi_u32 v0, v2, v0
	v_add_u32_e32 v0, v2, v0
	v_mul_hi_u32 v0, v3, v0
	v_mul_lo_u32 v1, v0, v9
	v_sub_u32_e32 v1, v3, v1
	v_add_u32_e32 v2, 1, v0
	v_cmp_ge_u32_e32 vcc, v1, v9
	s_nop 1
	v_cndmask_b32_e32 v0, v0, v2, vcc
	v_sub_u32_e32 v2, v1, v9
	v_cndmask_b32_e32 v1, v1, v2, vcc
	v_add_u32_e32 v2, 1, v0
	v_cmp_ge_u32_e32 vcc, v1, v9
	v_add_u32_e32 v1, 1, v3
	s_nop 0
	v_cndmask_b32_e32 v0, v0, v2, vcc
	v_mul_lo_u32 v2, v9, v0
	v_add_u32_e32 v2, v2, v9
	v_cmp_ne_u32_e32 vcc, v1, v2
	s_and_saveexec_b64 s[6:7], vcc
	s_xor_b64 s[6:7], exec, s[6:7]
	s_cbranch_execz .LBB0_101
	s_waitcnt lgkmcnt(0)
	v_add_u32_e32 v0, 1, v0
	v_mul_lo_u32 v0, v0, v8
	v_mov_b32_e32 v1, 0x3000
	global_load_dword v1, v1, s[28:29] offset:1024 sc1
	s_add_u32 s14, s28, 0x3400
	s_addc_u32 s15, s29, 0
	s_waitcnt vmcnt(0)
	v_cmp_lt_u32_e32 vcc, v1, v0
	s_and_saveexec_b64 s[12:13], vcc
	s_cbranch_execz .LBB0_100
	s_mov_b32 s3, 1
	s_mov_b64 s[16:17], 0
	v_mov_b32_e32 v1, 0
	v_mov_b32_e32 v2, 0
	s_branch .LBB0_91

; __device__ __forceinline__ unsigned xb_ld(unsigned* p)              { return __hip_atomic_load(p, __ATOMIC_RELAXED, __HIP_MEMORY_SCOPE_AGENT); }
; #define XB_SPIN(cond, bar) do { unsigned _sp = 0; while (cond) { __builtin_amdgcn_s_sleep(1); \
;     if ((++_sp & 255u) == 0u) { if (xb_ld(&(bar)[XB_TMO])) break; if (_sp > XB_SPIN_CAP) { atomicAdd(&(bar)[XB_TMO], 1u); break; } } } } while (0)
; __device__ __forceinline__ void xcd_barrier(const XcdBarrier& b, const bool xb_leader) {
;     ...
;             else XB_SPIN(xb_ld(&bar[XB_TOPGEN]) == tg, bar);
.LBB0_95:
	global_load_dword v2, v1, s[14:15] sc1
	s_add_i32 s3, s3, 1
	s_mov_b64 s[22:23], -1
	s_waitcnt vmcnt(1)
	v_cmp_ge_u32_e32 vcc, v2, v0
	s_orn2_b64 s[20:21], vcc, exec
	s_branch .LBB0_90

; __device__ __forceinline__ unsigned xb_ld(unsigned* p)              { return __hip_atomic_load(p, __ATOMIC_RELAXED, __HIP_MEMORY_SCOPE_AGENT); }
; #define XB_SPIN(cond, bar) do { unsigned _sp = 0; while (cond) { __builtin_amdgcn_s_sleep(1); \
;     if ((++_sp & 255u) == 0u) { if (xb_ld(&(bar)[XB_TMO])) break; if (_sp > XB_SPIN_CAP) { atomicAdd(&(bar)[XB_TMO], 1u); break; } } } } while (0)
; __device__ __forceinline__ void xcd_barrier(const XcdBarrier& b, const bool xb_leader) {
;     ...
;             XB_SPIN(xb_ld(&bar[XB_XGEN(b.x)]) == gen, bar);
.LBB0_112:
	global_load_dword v1, v0, s[12:13] sc1
	s_add_i32 s3, s3, 1
	s_mov_b64 s[22:23], -1
	s_waitcnt vmcnt(1)
	v_cmp_ge_u32_e32 vcc, v1, v4
	s_orn2_b64 s[26:27], vcc, exec
	s_branch .LBB0_107

; __device__ __forceinline__ unsigned xb_ld(unsigned* p)              { return __hip_atomic_load(p, __ATOMIC_RELAXED, __HIP_MEMORY_SCOPE_AGENT); }
; __device__ __forceinline__ unsigned xb_add(unsigned* p, unsigned v) { return __hip_atomic_fetch_add(p, v, __ATOMIC_RELAXED, __HIP_MEMORY_SCOPE_AGENT); }
; #define XB_SPIN(cond, bar) do { unsigned _sp = 0; while (cond) { __builtin_amdgcn_s_sleep(1); \
;     if ((++_sp & 255u) == 0u) { if (xb_ld(&(bar)[XB_TMO])) break; if (_sp > XB_SPIN_CAP) { atomicAdd(&(bar)[XB_TMO], 1u); break; } } } } while (0)
; __device__ __forceinline__ void xcc_barrier(unsigned* bar, unsigned* cnt, unsigned nloc, const bool xb_leader) {
;     asm volatile("s_waitcnt vmcnt(0)" ::: "memory");
;     __syncthreads();
;     if (xb_leader) {
;         __builtin_amdgcn_s_waitcnt(0);
;         const unsigned old = xb_add(cnt, 1u), target = (old / nloc + 1u) * nloc;
;         XB_SPIN(xb_ld(cnt) < target, bar);
.LBB0_137:
	s_or_b64 exec, exec, s[10:11]
	v_mov_b32_e32 v0, 0
	global_load_dword v3, v0, s[6:7] sc1
	s_ashr_i32 s3, s33, 31
	s_lshr_b32 s3, s3, 29
	s_add_i32 s3, s33, s3
	s_ashr_i32 s8, s3, 3
	v_cvt_f32_u32_e32 v4, s8
	s_sub_i32 s3, 0, s8
	s_waitcnt vmcnt(1)
	v_readfirstlane_b32 s9, v2
	v_rcp_iflag_f32_e32 v4, v4
	s_nop 0
	v_add_u32_e32 v1, s9, v1
	v_mul_f32_e32 v4, 0x4f7ffffe, v4
	v_cvt_u32_f32_e32 v4, v4
	v_mul_lo_u32 v2, s3, v4
	v_mul_hi_u32 v2, v4, v2
	v_add_u32_e32 v2, v4, v2
	v_mul_hi_u32 v2, v1, v2
	v_mul_lo_u32 v4, v2, s8
	v_sub_u32_e32 v1, v1, v4
	v_add_u32_e32 v4, 1, v2
	v_cmp_le_u32_e32 vcc, s8, v1
	s_mov_b32 s3, 1
	s_nop 0
	v_cndmask_b32_e32 v2, v2, v4, vcc
	v_subrev_u32_e32 v4, s8, v1
	v_cndmask_b32_e32 v1, v1, v4, vcc
	v_add_u32_e32 v4, 1, v2
	v_cmp_le_u32_e32 vcc, s8, v1
	s_nop 1
	v_cndmask_b32_e32 v1, v2, v4, vcc
	v_mul_lo_u32 v1, s8, v1
	v_add_u32_e32 v1, s8, v1
	s_waitcnt vmcnt(0)
	v_cmp_lt_u32_e32 vcc, v3, v1
	v_mov_b32_e32 v2, 0
	s_and_saveexec_b64 s[8:9], vcc
	s_cbranch_execz .LBB0_149
	s_mov_b64 s[10:11], 0
	s_branch .LBB0_140

; __device__ __forceinline__ unsigned xb_ld(unsigned* p)              { return __hip_atomic_load(p, __ATOMIC_RELAXED, __HIP_MEMORY_SCOPE_AGENT); }
; #define XB_SPIN(cond, bar) do { unsigned _sp = 0; while (cond) { __builtin_amdgcn_s_sleep(1); \
;     if ((++_sp & 255u) == 0u) { if (xb_ld(&(bar)[XB_TMO])) break; if (_sp > XB_SPIN_CAP) { atomicAdd(&(bar)[XB_TMO], 1u); break; } } } } while (0)
; __device__ __forceinline__ void xcc_barrier(unsigned* bar, unsigned* cnt, unsigned nloc, const bool xb_leader) {
;     ...
;         XB_SPIN(xb_ld(cnt) < target, bar);
.LBB0_144:
	global_load_dword v2, v0, s[6:7] sc1
	s_add_i32 s3, s3, 1
	s_mov_b64 s[16:17], -1
	s_waitcnt vmcnt(1)
	v_cmp_ge_u32_e32 vcc, v2, v1
	s_orn2_b64 s[14:15], vcc, exec
	s_branch .LBB0_139

; __device__ __forceinline__ unsigned xb_ld(unsigned* p)              { return __hip_atomic_load(p, __ATOMIC_RELAXED, __HIP_MEMORY_SCOPE_AGENT); }
; __device__ __forceinline__ unsigned xb_add(unsigned* p, unsigned v) { return __hip_atomic_fetch_add(p, v, __ATOMIC_RELAXED, __HIP_MEMORY_SCOPE_AGENT); }
; #define XB_SPIN(cond, bar) do { unsigned _sp = 0; while (cond) { __builtin_amdgcn_s_sleep(1); \
;     if ((++_sp & 255u) == 0u) { if (xb_ld(&(bar)[XB_TMO])) break; if (_sp > XB_SPIN_CAP) { atomicAdd(&(bar)[XB_TMO], 1u); break; } } } } while (0)
; __device__ __forceinline__ void xcd_barrier(const XcdBarrier& b, const bool xb_leader) {
;     ...
;         const unsigned old = xb_add(&bar[XB_XSUB(b.x)], 1u);
;         const unsigned gen = old / nloc;
;         if (old + 1u == (gen + 1u) * nloc) {
;             __builtin_amdgcn_fence(__ATOMIC_RELEASE, "agent");
;             asm volatile("s_waitcnt vmcnt(0)" ::: "memory");
;             const unsigned og = xb_add(&bar[XB_TOP], 1u);
;             const unsigned tg = og / nx;
;             if (og + 1u == (tg + 1u) * nx) xb_add(&bar[XB_TOPGEN], 1u);
;             else XB_SPIN(xb_ld(&bar[XB_TOPGEN]) == tg, bar);
.LBB0_180:
	s_or_b64 exec, exec, s[10:11]
	v_cvt_f32_u32_e32 v2, v9
	s_waitcnt vmcnt(0)
	v_readfirstlane_b32 s3, v1
	v_sub_u32_e32 v1, 0, v9
	v_rcp_iflag_f32_e32 v2, v2
	v_add_u32_e32 v3, s3, v0
	v_mul_f32_e32 v2, 0x4f7ffffe, v2
	v_cvt_u32_f32_e32 v2, v2
	v_mul_lo_u32 v0, v1, v2
	v_mul_hi_u32 v0, v2, v0
	v_add_u32_e32 v0, v2, v0
	v_mul_hi_u32 v0, v3, v0
	v_mul_lo_u32 v1, v0, v9
	v_sub_u32_e32 v1, v3, v1
	v_add_u32_e32 v2, 1, v0
	v_cmp_ge_u32_e32 vcc, v1, v9
	s_nop 1
	v_cndmask_b32_e32 v0, v0, v2, vcc
	v_sub_u32_e32 v2, v1, v9
	v_cndmask_b32_e32 v1, v1, v2, vcc
	v_add_u32_e32 v2, 1, v0
	v_cmp_ge_u32_e32 vcc, v1, v9
	v_add_u32_e32 v1, 1, v3
	s_nop 0
	v_cndmask_b32_e32 v0, v0, v2, vcc
	v_mul_lo_u32 v2, v9, v0
	v_add_u32_e32 v2, v2, v9
	v_cmp_ne_u32_e32 vcc, v1, v2
	s_and_saveexec_b64 s[8:9], vcc
	s_xor_b64 s[8:9], exec, s[8:9]
	s_cbranch_execz .LBB0_194
	s_waitcnt lgkmcnt(0)
	v_add_u32_e32 v0, 1, v0
	v_mul_lo_u32 v0, v0, v8
	v_mov_b32_e32 v1, 0x3000
	global_load_dword v1, v1, s[28:29] offset:1024 sc1
	s_add_u32 s12, s28, 0x3400
	s_addc_u32 s13, s29, 0
	s_waitcnt vmcnt(0)
	v_cmp_lt_u32_e32 vcc, v1, v0
	s_and_saveexec_b64 s[10:11], vcc
	s_cbranch_execz .LBB0_193
	s_mov_b32 s3, 1
	s_mov_b64 s[14:15], 0
	v_mov_b32_e32 v1, 0
	v_mov_b32_e32 v2, 0
	s_branch .LBB0_184

; __device__ __forceinline__ unsigned xb_ld(unsigned* p)              { return __hip_atomic_load(p, __ATOMIC_RELAXED, __HIP_MEMORY_SCOPE_AGENT); }
; #define XB_SPIN(cond, bar) do { unsigned _sp = 0; while (cond) { __builtin_amdgcn_s_sleep(1); \
;     if ((++_sp & 255u) == 0u) { if (xb_ld(&(bar)[XB_TMO])) break; if (_sp > XB_SPIN_CAP) { atomicAdd(&(bar)[XB_TMO], 1u); break; } } } } while (0)
; __device__ __forceinline__ void xcd_barrier(const XcdBarrier& b, const bool xb_leader) {
;     ...
;             else XB_SPIN(xb_ld(&bar[XB_TOPGEN]) == tg, bar);
.LBB0_188:
	global_load_dword v2, v1, s[12:13] sc1
	s_add_i32 s3, s3, 1
	s_mov_b64 s[20:21], -1
	s_waitcnt vmcnt(1)
	v_cmp_ge_u32_e32 vcc, v2, v0
	s_orn2_b64 s[18:19], vcc, exec
	s_branch .LBB0_183

; __device__ __forceinline__ unsigned xb_ld(unsigned* p)              { return __hip_atomic_load(p, __ATOMIC_RELAXED, __HIP_MEMORY_SCOPE_AGENT); }
; #define XB_SPIN(cond, bar) do { unsigned _sp = 0; while (cond) { __builtin_amdgcn_s_sleep(1); \
;     if ((++_sp & 255u) == 0u) { if (xb_ld(&(bar)[XB_TMO])) break; if (_sp > XB_SPIN_CAP) { atomicAdd(&(bar)[XB_TMO], 1u); break; } } } } while (0)
; __device__ __forceinline__ void xcd_barrier(const XcdBarrier& b, const bool xb_leader) {
;     ...
;             XB_SPIN(xb_ld(&bar[XB_XGEN(b.x)]) == gen, bar);
.LBB0_205:
	global_load_dword v1, v0, s[10:11] sc1
	s_add_i32 s3, s3, 1
	s_mov_b64 s[20:21], -1
	s_waitcnt vmcnt(1)
	v_cmp_ge_u32_e32 vcc, v1, v4
	s_orn2_b64 s[24:25], vcc, exec
	s_branch .LBB0_200

; __device__ __forceinline__ unsigned xb_ld(unsigned* p)              { return __hip_atomic_load(p, __ATOMIC_RELAXED, __HIP_MEMORY_SCOPE_AGENT); }
; __device__ __forceinline__ unsigned xb_add(unsigned* p, unsigned v) { return __hip_atomic_fetch_add(p, v, __ATOMIC_RELAXED, __HIP_MEMORY_SCOPE_AGENT); }
; #define XB_SPIN(cond, bar) do { unsigned _sp = 0; while (cond) { __builtin_amdgcn_s_sleep(1); \
;     if ((++_sp & 255u) == 0u) { if (xb_ld(&(bar)[XB_TMO])) break; if (_sp > XB_SPIN_CAP) { atomicAdd(&(bar)[XB_TMO], 1u); break; } } } } while (0)
; __device__ __forceinline__ void xcc_barrier(unsigned* bar, unsigned* cnt, unsigned nloc, const bool xb_leader) {
;     asm volatile("s_waitcnt vmcnt(0)" ::: "memory");
;     __syncthreads();
;     if (xb_leader) {
;         __builtin_amdgcn_s_waitcnt(0);
;         const unsigned old = xb_add(cnt, 1u), target = (old / nloc + 1u) * nloc;
;         XB_SPIN(xb_ld(cnt) < target, bar);
.LBB0_748:
	s_or_b64 exec, exec, s[8:9]
	v_mov_b32_e32 v0, 0
	global_load_dword v3, v0, s[4:5] sc1
	s_ashr_i32 s3, s33, 31
	s_lshr_b32 s3, s3, 29
	s_add_i32 s3, s33, s3
	s_ashr_i32 s6, s3, 3
	v_cvt_f32_u32_e32 v4, s6
	s_sub_i32 s3, 0, s6
	s_waitcnt vmcnt(1)
	v_readfirstlane_b32 s7, v2
	v_rcp_iflag_f32_e32 v4, v4
	s_nop 0
	v_add_u32_e32 v1, s7, v1
	v_mul_f32_e32 v4, 0x4f7ffffe, v4
	v_cvt_u32_f32_e32 v4, v4
	v_mul_lo_u32 v2, s3, v4
	v_mul_hi_u32 v2, v4, v2
	v_add_u32_e32 v2, v4, v2
	v_mul_hi_u32 v2, v1, v2
	v_mul_lo_u32 v4, v2, s6
	v_sub_u32_e32 v1, v1, v4
	v_add_u32_e32 v4, 1, v2
	v_cmp_le_u32_e32 vcc, s6, v1
	s_mov_b32 s3, 1
	s_nop 0
	v_cndmask_b32_e32 v2, v2, v4, vcc
	v_subrev_u32_e32 v4, s6, v1
	v_cndmask_b32_e32 v1, v1, v4, vcc
	v_add_u32_e32 v4, 1, v2
	v_cmp_le_u32_e32 vcc, s6, v1
	s_nop 1
	v_cndmask_b32_e32 v1, v2, v4, vcc
	v_mul_lo_u32 v1, s6, v1
	v_add_u32_e32 v1, s6, v1
	s_waitcnt vmcnt(0)
	v_cmp_lt_u32_e32 vcc, v3, v1
	v_mov_b32_e32 v2, 0
	s_and_saveexec_b64 s[6:7], vcc
	s_cbranch_execz .LBB0_790
	s_mov_b64 s[8:9], 0
	s_branch .LBB0_751

; __device__ __forceinline__ unsigned xb_ld(unsigned* p)              { return __hip_atomic_load(p, __ATOMIC_RELAXED, __HIP_MEMORY_SCOPE_AGENT); }
; #define XB_SPIN(cond, bar) do { unsigned _sp = 0; while (cond) { __builtin_amdgcn_s_sleep(1); \
;     if ((++_sp & 255u) == 0u) { if (xb_ld(&(bar)[XB_TMO])) break; if (_sp > XB_SPIN_CAP) { atomicAdd(&(bar)[XB_TMO], 1u); break; } } } } while (0)
; __device__ __forceinline__ void xcc_barrier(unsigned* bar, unsigned* cnt, unsigned nloc, const bool xb_leader) {
;     ...
;         XB_SPIN(xb_ld(cnt) < target, bar);
.LBB0_755:
	global_load_dword v2, v0, s[4:5] sc1
	s_add_i32 s3, s3, 1
	s_mov_b64 s[14:15], -1
	s_waitcnt vmcnt(1)
	v_cmp_ge_u32_e32 vcc, v2, v1
	s_orn2_b64 s[12:13], vcc, exec
	s_branch .LBB0_750

; __device__ __forceinline__ unsigned xb_ld(unsigned* p)              { return __hip_atomic_load(p, __ATOMIC_RELAXED, __HIP_MEMORY_SCOPE_AGENT); }
; __device__ __forceinline__ unsigned xb_add(unsigned* p, unsigned v) { return __hip_atomic_fetch_add(p, v, __ATOMIC_RELAXED, __HIP_MEMORY_SCOPE_AGENT); }
; #define XB_SPIN(cond, bar) do { unsigned _sp = 0; while (cond) { __builtin_amdgcn_s_sleep(1); \
;     if ((++_sp & 255u) == 0u) { if (xb_ld(&(bar)[XB_TMO])) break; if (_sp > XB_SPIN_CAP) { atomicAdd(&(bar)[XB_TMO], 1u); break; } } } } while (0)
; __device__ __forceinline__ void xcd_barrier(const XcdBarrier& b, const bool xb_leader) {
;     ...
;         const unsigned old = xb_add(&bar[XB_XSUB(b.x)], 1u);
;         const unsigned gen = old / nloc;
;         if (old + 1u == (gen + 1u) * nloc) {
;             __builtin_amdgcn_fence(__ATOMIC_RELEASE, "agent");
;             asm volatile("s_waitcnt vmcnt(0)" ::: "memory");
;             const unsigned og = xb_add(&bar[XB_TOP], 1u);
;             const unsigned tg = og / nx;
;             if (og + 1u == (tg + 1u) * nx) xb_add(&bar[XB_TOPGEN], 1u);
;             else XB_SPIN(xb_ld(&bar[XB_TOPGEN]) == tg, bar);
.LBB0_821:
	s_or_b64 exec, exec, s[8:9]
	v_cvt_f32_u32_e32 v2, v9
	s_waitcnt vmcnt(0)
	v_readfirstlane_b32 s3, v1
	v_sub_u32_e32 v1, 0, v9
	v_rcp_iflag_f32_e32 v2, v2
	v_add_u32_e32 v3, s3, v0
	v_mul_f32_e32 v2, 0x4f7ffffe, v2
	v_cvt_u32_f32_e32 v2, v2
	v_mul_lo_u32 v0, v1, v2
	v_mul_hi_u32 v0, v2, v0
	v_add_u32_e32 v0, v2, v0
	v_mul_hi_u32 v0, v3, v0
	v_mul_lo_u32 v1, v0, v9
	v_sub_u32_e32 v1, v3, v1
	v_add_u32_e32 v2, 1, v0
	v_cmp_ge_u32_e32 vcc, v1, v9
	s_nop 1
	v_cndmask_b32_e32 v0, v0, v2, vcc
	v_sub_u32_e32 v2, v1, v9
	v_cndmask_b32_e32 v1, v1, v2, vcc
	v_add_u32_e32 v2, 1, v0
	v_cmp_ge_u32_e32 vcc, v1, v9
	v_add_u32_e32 v1, 1, v3
	s_nop 0
	v_cndmask_b32_e32 v0, v0, v2, vcc
	v_mul_lo_u32 v2, v9, v0
	v_add_u32_e32 v2, v2, v9
	v_cmp_ne_u32_e32 vcc, v1, v2
	s_and_saveexec_b64 s[6:7], vcc
	s_xor_b64 s[6:7], exec, s[6:7]
	s_cbranch_execz .LBB0_835
	s_waitcnt lgkmcnt(0)
	v_add_u32_e32 v0, 1, v0
	v_mul_lo_u32 v0, v0, v8
	v_mov_b32_e32 v1, 0x3000
	global_load_dword v1, v1, s[28:29] offset:1024 sc1
	s_add_u32 s10, s28, 0x3400
	s_addc_u32 s11, s29, 0
	s_waitcnt vmcnt(0)
	v_cmp_lt_u32_e32 vcc, v1, v0
	s_and_saveexec_b64 s[8:9], vcc
	s_cbranch_execz .LBB0_834
	s_mov_b32 s3, 1
	s_mov_b64 s[12:13], 0
	v_mov_b32_e32 v1, 0
	v_mov_b32_e32 v2, 0
	s_branch .LBB0_825

; __device__ __forceinline__ unsigned xb_ld(unsigned* p)              { return __hip_atomic_load(p, __ATOMIC_RELAXED, __HIP_MEMORY_SCOPE_AGENT); }
; #define XB_SPIN(cond, bar) do { unsigned _sp = 0; while (cond) { __builtin_amdgcn_s_sleep(1); \
;     if ((++_sp & 255u) == 0u) { if (xb_ld(&(bar)[XB_TMO])) break; if (_sp > XB_SPIN_CAP) { atomicAdd(&(bar)[XB_TMO], 1u); break; } } } } while (0)
; __device__ __forceinline__ void xcd_barrier(const XcdBarrier& b, const bool xb_leader) {
;     ...
;             else XB_SPIN(xb_ld(&bar[XB_TOPGEN]) == tg, bar);
.LBB0_829:
	global_load_dword v2, v1, s[10:11] sc1
	s_add_i32 s3, s3, 1
	s_mov_b64 s[20:21], -1
	s_waitcnt vmcnt(1)
	v_cmp_ge_u32_e32 vcc, v2, v0
	s_orn2_b64 s[16:17], vcc, exec
	s_branch .LBB0_824

; __device__ __forceinline__ unsigned xb_ld(unsigned* p)              { return __hip_atomic_load(p, __ATOMIC_RELAXED, __HIP_MEMORY_SCOPE_AGENT); }
; #define XB_SPIN(cond, bar) do { unsigned _sp = 0; while (cond) { __builtin_amdgcn_s_sleep(1); \
;     if ((++_sp & 255u) == 0u) { if (xb_ld(&(bar)[XB_TMO])) break; if (_sp > XB_SPIN_CAP) { atomicAdd(&(bar)[XB_TMO], 1u); break; } } } } while (0)
; __device__ __forceinline__ void xcd_barrier(const XcdBarrier& b, const bool xb_leader) {
;     ...
;             XB_SPIN(xb_ld(&bar[XB_XGEN(b.x)]) == gen, bar);
.LBB0_846:
	global_load_dword v1, v0, s[8:9] sc1
	s_add_i32 s3, s3, 1
	s_mov_b64 s[20:21], -1
	s_waitcnt vmcnt(1)
	v_cmp_ge_u32_e32 vcc, v1, v4
	s_orn2_b64 s[24:25], vcc, exec
	s_branch .LBB0_841

; __device__ __forceinline__ unsigned xb_ld(unsigned* p)              { return __hip_atomic_load(p, __ATOMIC_RELAXED, __HIP_MEMORY_SCOPE_AGENT); }
; #define XB_SPIN(cond, bar) do { unsigned _sp = 0; while (cond) { __builtin_amdgcn_s_sleep(1); \
;     if ((++_sp & 255u) == 0u) { if (xb_ld(&(bar)[XB_TMO])) break; if (_sp > XB_SPIN_CAP) { atomicAdd(&(bar)[XB_TMO], 1u); break; } } } } while (0)
; __device__ __forceinline__ void xcd_barrier(const XcdBarrier& b, const bool xb_leader) {
;     ...
;             else XB_SPIN(xb_ld(&bar[XB_TOPGEN]) == tg, bar);
.LBB0_932:
	global_load_dword v2, v1, s[12:13] sc1
	s_add_i32 s3, s3, 1
	s_mov_b64 s[24:25], -1
	s_waitcnt vmcnt(1)
	v_cmp_ge_u32_e32 vcc, v2, v0
	s_orn2_b64 s[22:23], vcc, exec
	s_branch .LBB0_927

; __device__ __forceinline__ unsigned xb_ld(unsigned* p)              { return __hip_atomic_load(p, __ATOMIC_RELAXED, __HIP_MEMORY_SCOPE_AGENT); }
; #define XB_SPIN(cond, bar) do { unsigned _sp = 0; while (cond) { __builtin_amdgcn_s_sleep(1); \
;     if ((++_sp & 255u) == 0u) { if (xb_ld(&(bar)[XB_TMO])) break; if (_sp > XB_SPIN_CAP) { atomicAdd(&(bar)[XB_TMO], 1u); break; } } } } while (0)
; __device__ __forceinline__ void xcd_barrier(const XcdBarrier& b, const bool xb_leader) {
;     ...
;             XB_SPIN(xb_ld(&bar[XB_XGEN(b.x)]) == gen, bar);
.LBB0_949:
	global_load_dword v1, v0, s[10:11] sc1
	s_add_i32 s3, s3, 1
	s_mov_b64 s[24:25], -1
	s_waitcnt vmcnt(1)
	v_cmp_ge_u32_e32 vcc, v1, v4
	s_orn2_b64 s[30:31], vcc, exec
	s_branch .LBB0_944

; __device__ __forceinline__ unsigned xb_ld(unsigned* p)              { return __hip_atomic_load(p, __ATOMIC_RELAXED, __HIP_MEMORY_SCOPE_AGENT); }
; #define XB_SPIN(cond, bar) do { unsigned _sp = 0; while (cond) { __builtin_amdgcn_s_sleep(1); \
;     if ((++_sp & 255u) == 0u) { if (xb_ld(&(bar)[XB_TMO])) break; if (_sp > XB_SPIN_CAP) { atomicAdd(&(bar)[XB_TMO], 1u); break; } } } } while (0)
; __device__ __forceinline__ void xcd_barrier(const XcdBarrier& b, const bool xb_leader) {
;     ...
;             else XB_SPIN(xb_ld(&bar[XB_TOPGEN]) == tg, bar);
.LBB0_1082:
	global_load_dword v2, v1, s[10:11] sc1
	s_add_i32 s3, s3, 1
	s_mov_b64 s[24:25], -1
	s_waitcnt vmcnt(1)
	v_cmp_ge_u32_e32 vcc, v2, v0
	s_orn2_b64 s[16:17], vcc, exec
	s_branch .LBB0_1077

; __device__ __forceinline__ unsigned xb_ld(unsigned* p)              { return __hip_atomic_load(p, __ATOMIC_RELAXED, __HIP_MEMORY_SCOPE_AGENT); }
; #define XB_SPIN(cond, bar) do { unsigned _sp = 0; while (cond) { __builtin_amdgcn_s_sleep(1); \
;     if ((++_sp & 255u) == 0u) { if (xb_ld(&(bar)[XB_TMO])) break; if (_sp > XB_SPIN_CAP) { atomicAdd(&(bar)[XB_TMO], 1u); break; } } } } while (0)
; __device__ __forceinline__ void xcd_barrier(const XcdBarrier& b, const bool xb_leader) {
;     ...
;             XB_SPIN(xb_ld(&bar[XB_XGEN(b.x)]) == gen, bar);
.LBB0_1099:
	global_load_dword v1, v0, s[8:9] sc1
	s_add_i32 s3, s3, 1
	s_mov_b64 s[24:25], -1
	s_waitcnt vmcnt(1)
	v_cmp_ge_u32_e32 vcc, v1, v4
	s_orn2_b64 s[30:31], vcc, exec
	s_branch .LBB0_1094

; __device__ __forceinline__ unsigned xb_ld(unsigned* p)              { return __hip_atomic_load(p, __ATOMIC_RELAXED, __HIP_MEMORY_SCOPE_AGENT); }
; __device__ __forceinline__ unsigned xb_add(unsigned* p, unsigned v) { return __hip_atomic_fetch_add(p, v, __ATOMIC_RELAXED, __HIP_MEMORY_SCOPE_AGENT); }
; #define XB_SPIN(cond, bar) do { unsigned _sp = 0; while (cond) { __builtin_amdgcn_s_sleep(1); \
;     if ((++_sp & 255u) == 0u) { if (xb_ld(&(bar)[XB_TMO])) break; if (_sp > XB_SPIN_CAP) { atomicAdd(&(bar)[XB_TMO], 1u); break; } } } } while (0)
; __device__ __forceinline__ void xcd_barrier(const XcdBarrier& b, const bool xb_leader) {
;     ...
;         const unsigned old = xb_add(&bar[XB_XSUB(b.x)], 1u);
;         const unsigned gen = old / nloc;
;         if (old + 1u == (gen + 1u) * nloc) {
;             __builtin_amdgcn_fence(__ATOMIC_RELEASE, "agent");
;             asm volatile("s_waitcnt vmcnt(0)" ::: "memory");
;             const unsigned og = xb_add(&bar[XB_TOP], 1u);
;             const unsigned tg = og / nx;
;             if (og + 1u == (tg + 1u) * nx) xb_add(&bar[XB_TOPGEN], 1u);
;             else XB_SPIN(xb_ld(&bar[XB_TOPGEN]) == tg, bar);
;             __builtin_amdgcn_fence(__ATOMIC_ACQUIRE, "agent");
;             xb_add(&bar[XB_XGEN(b.x)], 1u);
;             asm volatile("s_waitcnt vmcnt(0)" ::: "memory");
;         } else {
;             XB_SPIN(xb_ld(&bar[XB_XGEN(b.x)]) == gen, bar);
.LBB0_1213:
	s_or_b64 exec, exec, s[10:11]
	v_cvt_f32_u32_e32 v2, v9
	s_waitcnt vmcnt(0)
	v_readfirstlane_b32 s3, v1
	v_sub_u32_e32 v1, 0, v9
	v_rcp_iflag_f32_e32 v2, v2
	v_add_u32_e32 v3, s3, v0
	v_mul_f32_e32 v2, 0x4f7ffffe, v2
	v_cvt_u32_f32_e32 v2, v2
	v_mul_lo_u32 v0, v1, v2
	v_mul_hi_u32 v0, v2, v0
	v_add_u32_e32 v0, v2, v0
	v_mul_hi_u32 v0, v3, v0
	v_mul_lo_u32 v1, v0, v9
	v_sub_u32_e32 v1, v3, v1
	v_add_u32_e32 v2, 1, v0
	v_cmp_ge_u32_e32 vcc, v1, v9
	s_nop 1
	v_cndmask_b32_e32 v0, v0, v2, vcc
	v_sub_u32_e32 v2, v1, v9
	v_cndmask_b32_e32 v1, v1, v2, vcc
	v_add_u32_e32 v2, 1, v0
	v_cmp_ge_u32_e32 vcc, v1, v9
	v_add_u32_e32 v1, 1, v3
	s_nop 0
	v_cndmask_b32_e32 v0, v0, v2, vcc
	v_mul_lo_u32 v2, v9, v0
	v_add_u32_e32 v2, v2, v9
	v_cmp_ne_u32_e32 vcc, v1, v2
	s_and_saveexec_b64 s[8:9], vcc
	s_xor_b64 s[8:9], exec, s[8:9]
	s_cbranch_execz .LBB0_1227
	s_waitcnt lgkmcnt(0)
	v_add_u32_e32 v0, 1, v0
	v_mul_lo_u32 v0, v0, v8
	v_mov_b32_e32 v1, 0x3000
	global_load_dword v1, v1, s[28:29] offset:1024 sc1
	s_add_u32 s12, s28, 0x3400
	s_addc_u32 s13, s29, 0
	s_waitcnt vmcnt(0)
	v_cmp_lt_u32_e32 vcc, v1, v0
	s_andn2_b64 vcc, vcc, s[98:99]
	s_and_saveexec_b64 s[10:11], vcc
	s_cbranch_execz .LBB0_1226
	s_mov_b32 s3, 1
	s_mov_b64 s[14:15], 0
	v_mov_b32_e32 v1, 0
	v_mov_b32_e32 v2, 0
	s_branch .LBB0_1217

; __device__ __forceinline__ unsigned xb_ld(unsigned* p)              { return __hip_atomic_load(p, __ATOMIC_RELAXED, __HIP_MEMORY_SCOPE_AGENT); }
; #define XB_SPIN(cond, bar) do { unsigned _sp = 0; while (cond) { __builtin_amdgcn_s_sleep(1); \
;     if ((++_sp & 255u) == 0u) { if (xb_ld(&(bar)[XB_TMO])) break; if (_sp > XB_SPIN_CAP) { atomicAdd(&(bar)[XB_TMO], 1u); break; } } } } while (0)
; __device__ __forceinline__ void xcd_barrier(const XcdBarrier& b, const bool xb_leader) {
;     ...
;             XB_SPIN(xb_ld(&bar[XB_XGEN(b.x)]) == gen, bar);
.LBB0_1221:
	global_load_dword v2, v1, s[12:13] sc1
	s_add_i32 s3, s3, 1
	s_mov_b64 s[26:27], -1
	s_waitcnt vmcnt(1)
	v_cmp_ge_u32_e32 vcc, v2, v0
	s_orn2_b64 s[24:25], vcc, exec
	s_branch .LBB0_1216

; __device__ __forceinline__ unsigned xb_ld(unsigned* p)              { return __hip_atomic_load(p, __ATOMIC_RELAXED, __HIP_MEMORY_SCOPE_AGENT); }
; #define XB_SPIN(cond, bar) do { unsigned _sp = 0; while (cond) { __builtin_amdgcn_s_sleep(1); \
;     if ((++_sp & 255u) == 0u) { if (xb_ld(&(bar)[XB_TMO])) break; if (_sp > XB_SPIN_CAP) { atomicAdd(&(bar)[XB_TMO], 1u); break; } } } } while (0)
; __device__ __forceinline__ void xcd_barrier(const XcdBarrier& b, const bool xb_leader) {
;     ...
;             else XB_SPIN(xb_ld(&bar[XB_TOPGEN]) == tg, bar);
.LBB0_1238:
	global_load_dword v1, v0, s[10:11] sc1
	s_add_i32 s3, s3, 1
	s_mov_b64 s[26:27], -1
	s_waitcnt vmcnt(1)
	v_cmp_ge_u32_e32 vcc, v1, v4
	s_orn2_b64 s[36:37], vcc, exec
	s_branch .LBB0_1233

; __device__ __forceinline__ unsigned xb_ld(unsigned* p)              { return __hip_atomic_load(p, __ATOMIC_RELAXED, __HIP_MEMORY_SCOPE_AGENT); }
; __device__ __forceinline__ unsigned xb_add(unsigned* p, unsigned v) { return __hip_atomic_fetch_add(p, v, __ATOMIC_RELAXED, __HIP_MEMORY_SCOPE_AGENT); }
; #define XB_SPIN(cond, bar) do { unsigned _sp = 0; while (cond) { __builtin_amdgcn_s_sleep(1); \
;     if ((++_sp & 255u) == 0u) { if (xb_ld(&(bar)[XB_TMO])) break; if (_sp > XB_SPIN_CAP) { atomicAdd(&(bar)[XB_TMO], 1u); break; } } } } while (0)
; __device__ __forceinline__ void xcc_barrier(unsigned* bar, unsigned* cnt, unsigned nloc, const bool xb_leader) {
;     asm volatile("s_waitcnt vmcnt(0)" ::: "memory");
;     __syncthreads();
;     if (xb_leader) {
;         __builtin_amdgcn_s_waitcnt(0);
;         const unsigned old = xb_add(cnt, 1u), target = (old / nloc + 1u) * nloc;
;         XB_SPIN(xb_ld(cnt) < target, bar);
.LBB0_1549:
	s_or_b64 exec, exec, s[10:11]
	v_mov_b32_e32 v0, 0
	global_load_dword v3, v0, s[4:5] sc1
	s_ashr_i32 s3, s33, 31
	s_lshr_b32 s3, s3, 29
	s_add_i32 s3, s33, s3
	s_ashr_i32 s6, s3, 3
	v_cvt_f32_u32_e32 v4, s6
	s_sub_i32 s3, 0, s6
	s_waitcnt vmcnt(1)
	v_readfirstlane_b32 s7, v2
	v_rcp_iflag_f32_e32 v4, v4
	s_nop 0
	v_add_u32_e32 v1, s7, v1
	v_mul_f32_e32 v4, 0x4f7ffffe, v4
	v_cvt_u32_f32_e32 v4, v4
	v_mul_lo_u32 v2, s3, v4
	v_mul_hi_u32 v2, v4, v2
	v_add_u32_e32 v2, v4, v2
	v_mul_hi_u32 v2, v1, v2
	v_mul_lo_u32 v4, v2, s6
	v_sub_u32_e32 v1, v1, v4
	v_add_u32_e32 v4, 1, v2
	v_cmp_le_u32_e32 vcc, s6, v1
	s_mov_b32 s3, 1
	s_nop 0
	v_cndmask_b32_e32 v2, v2, v4, vcc
	v_subrev_u32_e32 v4, s6, v1
	v_cndmask_b32_e32 v1, v1, v4, vcc
	v_add_u32_e32 v4, 1, v2
	v_cmp_le_u32_e32 vcc, s6, v1
	s_nop 1
	v_cndmask_b32_e32 v1, v2, v4, vcc
	v_mul_lo_u32 v1, s6, v1
	v_add_u32_e32 v1, s6, v1
	s_waitcnt vmcnt(0)
	v_cmp_lt_u32_e32 vcc, v3, v1
	v_mov_b32_e32 v2, 0
	s_and_saveexec_b64 s[6:7], vcc
	s_cbranch_execz .LBB0_1561
	s_mov_b64 s[10:11], 0
	s_branch .LBB0_1552

; __device__ __forceinline__ unsigned xb_ld(unsigned* p)              { return __hip_atomic_load(p, __ATOMIC_RELAXED, __HIP_MEMORY_SCOPE_AGENT); }
; #define XB_SPIN(cond, bar) do { unsigned _sp = 0; while (cond) { __builtin_amdgcn_s_sleep(1); \
;     if ((++_sp & 255u) == 0u) { if (xb_ld(&(bar)[XB_TMO])) break; if (_sp > XB_SPIN_CAP) { atomicAdd(&(bar)[XB_TMO], 1u); break; } } } } while (0)
; __device__ __forceinline__ void xcc_barrier(unsigned* bar, unsigned* cnt, unsigned nloc, const bool xb_leader) {
;     ...
;         XB_SPIN(xb_ld(cnt) < target, bar);
.LBB0_1556:
	global_load_dword v2, v0, s[4:5] sc1
	s_add_i32 s3, s3, 1
	s_mov_b64 s[16:17], -1
	s_waitcnt vmcnt(1)
	v_cmp_ge_u32_e32 vcc, v2, v1
	s_orn2_b64 s[14:15], vcc, exec
	s_branch .LBB0_1551

; __device__ __forceinline__ unsigned xb_ld(unsigned* p)              { return __hip_atomic_load(p, __ATOMIC_RELAXED, __HIP_MEMORY_SCOPE_AGENT); }
; __device__ __forceinline__ unsigned xb_add(unsigned* p, unsigned v) { return __hip_atomic_fetch_add(p, v, __ATOMIC_RELAXED, __HIP_MEMORY_SCOPE_AGENT); }
; #define XB_SPIN(cond, bar) do { unsigned _sp = 0; while (cond) { __builtin_amdgcn_s_sleep(1); \
;     if ((++_sp & 255u) == 0u) { if (xb_ld(&(bar)[XB_TMO])) break; if (_sp > XB_SPIN_CAP) { atomicAdd(&(bar)[XB_TMO], 1u); break; } } } } while (0)
; __device__ __forceinline__ void xcd_barrier(const XcdBarrier& b, const bool xb_leader) {
;     ...
;         const unsigned old = xb_add(&bar[XB_XSUB(b.x)], 1u);
;         const unsigned gen = old / nloc;
;         if (old + 1u == (gen + 1u) * nloc) {
;             __builtin_amdgcn_fence(__ATOMIC_RELEASE, "agent");
;             asm volatile("s_waitcnt vmcnt(0)" ::: "memory");
;             const unsigned og = xb_add(&bar[XB_TOP], 1u);
;             const unsigned tg = og / nx;
;             if (og + 1u == (tg + 1u) * nx) xb_add(&bar[XB_TOPGEN], 1u);
;             else XB_SPIN(xb_ld(&bar[XB_TOPGEN]) == tg, bar);
;             __builtin_amdgcn_fence(__ATOMIC_ACQUIRE, "agent");
;             xb_add(&bar[XB_XGEN(b.x)], 1u);
;             asm volatile("s_waitcnt vmcnt(0)" ::: "memory");
;         } else {
;             XB_SPIN(xb_ld(&bar[XB_XGEN(b.x)]) == gen, bar);
.LBB0_1592:
	s_or_b64 exec, exec, s[10:11]
	v_cvt_f32_u32_e32 v2, v9
	s_waitcnt vmcnt(0)
	v_readfirstlane_b32 s3, v1
	v_sub_u32_e32 v1, 0, v9
	v_rcp_iflag_f32_e32 v2, v2
	v_add_u32_e32 v3, s3, v0
	v_mul_f32_e32 v2, 0x4f7ffffe, v2
	v_cvt_u32_f32_e32 v2, v2
	v_mul_lo_u32 v0, v1, v2
	v_mul_hi_u32 v0, v2, v0
	v_add_u32_e32 v0, v2, v0
	v_mul_hi_u32 v0, v3, v0
	v_mul_lo_u32 v1, v0, v9
	v_sub_u32_e32 v1, v3, v1
	v_add_u32_e32 v2, 1, v0
	v_cmp_ge_u32_e32 vcc, v1, v9
	s_nop 1
	v_cndmask_b32_e32 v0, v0, v2, vcc
	v_sub_u32_e32 v2, v1, v9
	v_cndmask_b32_e32 v1, v1, v2, vcc
	v_add_u32_e32 v2, 1, v0
	v_cmp_ge_u32_e32 vcc, v1, v9
	v_add_u32_e32 v1, 1, v3
	s_nop 0
	v_cndmask_b32_e32 v0, v0, v2, vcc
	v_mul_lo_u32 v2, v9, v0
	v_add_u32_e32 v2, v2, v9
	v_cmp_ne_u32_e32 vcc, v1, v2
	s_and_saveexec_b64 s[6:7], vcc
	s_xor_b64 s[6:7], exec, s[6:7]
	s_cbranch_execz .LBB0_1606
	s_waitcnt lgkmcnt(0)
	v_add_u32_e32 v0, 1, v0
	v_mul_lo_u32 v0, v0, v8
	v_mov_b32_e32 v1, 0x3000
	global_load_dword v1, v1, s[28:29] offset:1024 sc1
	s_add_u32 s12, s28, 0x3400
	s_addc_u32 s13, s29, 0
	s_waitcnt vmcnt(0)
	v_cmp_lt_u32_e32 vcc, v1, v0
	s_and_saveexec_b64 s[10:11], vcc
	s_cbranch_execz .LBB0_1605
	s_mov_b32 s3, 1
	s_mov_b64 s[14:15], 0
	v_mov_b32_e32 v1, 0
	v_mov_b32_e32 v2, 0
	s_branch .LBB0_1596

; __device__ __forceinline__ unsigned xb_ld(unsigned* p)              { return __hip_atomic_load(p, __ATOMIC_RELAXED, __HIP_MEMORY_SCOPE_AGENT); }
; __device__ __forceinline__ unsigned xb_add(unsigned* p, unsigned v) { return __hip_atomic_fetch_add(p, v, __ATOMIC_RELAXED, __HIP_MEMORY_SCOPE_AGENT); }
; #define XB_SPIN(cond, bar) do { unsigned _sp = 0; while (cond) { __builtin_amdgcn_s_sleep(1); \
;     if ((++_sp & 255u) == 0u) { if (xb_ld(&(bar)[XB_TMO])) break; if (_sp > XB_SPIN_CAP) { atomicAdd(&(bar)[XB_TMO], 1u); break; } } } } while (0)
; __device__ __forceinline__ void xcd_barrier(const XcdBarrier& b, const bool xb_leader) {
;     ...
;         const unsigned old = xb_add(&bar[XB_XSUB(b.x)], 1u);
;         const unsigned gen = old / nloc;
;         if (old + 1u == (gen + 1u) * nloc) {
;             __builtin_amdgcn_fence(__ATOMIC_RELEASE, "agent");
;             asm volatile("s_waitcnt vmcnt(0)" ::: "memory");
;             const unsigned og = xb_add(&bar[XB_TOP], 1u);
;             const unsigned tg = og / nx;
;             if (og + 1u == (tg + 1u) * nx) xb_add(&bar[XB_TOPGEN], 1u);
;             else XB_SPIN(xb_ld(&bar[XB_TOPGEN]) == tg, bar);
;             __builtin_amdgcn_fence(__ATOMIC_ACQUIRE, "agent");
;             xb_add(&bar[XB_XGEN(b.x)], 1u);
;             asm volatile("s_waitcnt vmcnt(0)" ::: "memory");
;         } else {
;             XB_SPIN(xb_ld(&bar[XB_XGEN(b.x)]) == gen, bar);
.LBB0_1908:
	s_or_b64 exec, exec, s[8:9]
	v_cvt_f32_u32_e32 v2, v9
	s_waitcnt vmcnt(0)
	v_readfirstlane_b32 s2, v1
	v_sub_u32_e32 v1, 0, v9
	v_rcp_iflag_f32_e32 v2, v2
	v_add_u32_e32 v3, s2, v0
	v_mul_f32_e32 v2, 0x4f7ffffe, v2
	v_cvt_u32_f32_e32 v2, v2
	v_mul_lo_u32 v0, v1, v2
	v_mul_hi_u32 v0, v2, v0
	v_add_u32_e32 v0, v2, v0
	v_mul_hi_u32 v0, v3, v0
	v_mul_lo_u32 v1, v0, v9
	v_sub_u32_e32 v1, v3, v1
	v_add_u32_e32 v2, 1, v0
	v_cmp_ge_u32_e32 vcc, v1, v9
	s_nop 1
	v_cndmask_b32_e32 v0, v0, v2, vcc
	v_sub_u32_e32 v2, v1, v9
	v_cndmask_b32_e32 v1, v1, v2, vcc
	v_add_u32_e32 v2, 1, v0
	v_cmp_ge_u32_e32 vcc, v1, v9
	v_add_u32_e32 v1, 1, v3
	s_nop 0
	v_cndmask_b32_e32 v0, v0, v2, vcc
	v_mul_lo_u32 v2, v9, v0
	v_add_u32_e32 v2, v2, v9
	v_cmp_ne_u32_e32 vcc, v1, v2
	s_and_saveexec_b64 s[2:3], vcc
	s_xor_b64 s[2:3], exec, s[2:3]
	s_cbranch_execz .LBB0_1922
	s_waitcnt lgkmcnt(0)
	v_add_u32_e32 v0, 1, v0
	v_mul_lo_u32 v0, v0, v8
	v_mov_b32_e32 v1, 0x3000
	global_load_dword v1, v1, s[28:29] offset:1024 sc1
	s_add_u32 s12, s28, 0x3400
	s_addc_u32 s13, s29, 0
	s_waitcnt vmcnt(0)
	v_cmp_lt_u32_e32 vcc, v1, v0
	s_and_saveexec_b64 s[8:9], vcc
	s_cbranch_execz .LBB0_1921
	s_mov_b32 s26, 1
	s_mov_b64 s[14:15], 0
	v_mov_b32_e32 v1, 0
	v_mov_b32_e32 v2, 0
	s_branch .LBB0_1912

; __device__ __forceinline__ unsigned xb_ld(unsigned* p)              { return __hip_atomic_load(p, __ATOMIC_RELAXED, __HIP_MEMORY_SCOPE_AGENT); }
; #define XB_SPIN(cond, bar) do { unsigned _sp = 0; while (cond) { __builtin_amdgcn_s_sleep(1); \
;     if ((++_sp & 255u) == 0u) { if (xb_ld(&(bar)[XB_TMO])) break; if (_sp > XB_SPIN_CAP) { atomicAdd(&(bar)[XB_TMO], 1u); break; } } } } while (0)
; __device__ __forceinline__ void xcd_barrier(const XcdBarrier& b, const bool xb_leader) {
;     ...
;             XB_SPIN(xb_ld(&bar[XB_XGEN(b.x)]) == gen, bar);
.LBB0_1916:
	global_load_dword v2, v1, s[12:13] sc1
	s_add_i32 s26, s26, 1
	s_mov_b64 s[22:23], -1
	s_waitcnt vmcnt(1)
	v_cmp_ge_u32_e32 vcc, v2, v0
	s_orn2_b64 s[20:21], vcc, exec
	s_branch .LBB0_1911

; __device__ __forceinline__ unsigned xb_ld(unsigned* p)              { return __hip_atomic_load(p, __ATOMIC_RELAXED, __HIP_MEMORY_SCOPE_AGENT); }
; #define XB_SPIN(cond, bar) do { unsigned _sp = 0; while (cond) { __builtin_amdgcn_s_sleep(1); \
;     if ((++_sp & 255u) == 0u) { if (xb_ld(&(bar)[XB_TMO])) break; if (_sp > XB_SPIN_CAP) { atomicAdd(&(bar)[XB_TMO], 1u); break; } } } } while (0)
; __device__ __forceinline__ void xcd_barrier(const XcdBarrier& b, const bool xb_leader) {
;     ...
;             else XB_SPIN(xb_ld(&bar[XB_TOPGEN]) == tg, bar);
.LBB0_1933:
	global_load_dword v1, v0, s[8:9] sc1
	s_add_i32 s28, s28, 1
	s_mov_b64 s[22:23], -1
	s_waitcnt vmcnt(1)
	v_cmp_ge_u32_e32 vcc, v1, v4
	s_orn2_b64 s[26:27], vcc, exec
	s_branch .LBB0_1928
